# T10 A + drain seam also takes the shares of absent workgroups when the grid is smaller than 256 (robustness; same timing path at 256)
# speedup vs baseline: 1.0039x; 1.0039x over previous
; __device__ __forceinline__ void moe_convert(Frame& F, int lo, int hi, int rank, int nrank) {
;     if (MOE_DMA) { moe_convert_dma(F, lo, hi, rank, nrank); return; }
;     for (int it = lo + rank; it < hi; it += nrank) {
;         int r = it; const float* W; unsigned char* WT; int N, ldt, kind, off; float f8s;
;         if (r < 14336) { const int e = r / 1792; r -= e * 1792; W = F.in[IN_WMG] + (size_t)e * 2048 * DFFE; N = DFFE; WT = F.ws + WS_WGU1 + (size_t)e * 14336 * 2048; ldt = 2048; kind = 1; off = 0; f8s = 32.f; }
;         else if ((r -= 14336) < 14336) { const int e = r / 1792; r -= e * 1792; W = F.in[IN_WMU] + (size_t)e * 2048 * DFFE; N = DFFE; WT = F.ws + WS_WGU1 + (size_t)e * 14336 * 2048; ldt = 2048; kind = 1; off = 128; f8s = 256.f; }
;         else { r -= 14336; const int e = r / 1792; r -= e * 1792; W = F.in[IN_WMD] + (size_t)e * DFFE * 2048; N = 2048; WT = F.ws + WS_WDN1 + (size_t)e * 2048 * DFFE; ldt = DFFE; kind = 0; off = 0; f8s = 64.f; }
;         transpose_item_f8(W, N, WT, ldt, kind, off, r, F.lane, f8s);
.Lsf15_notw0:
	s_cmp_gt_u32 s4, 4
	s_cbranch_scc1 .Lsf15_skip
	v_mov_b32_e32 v8, 0x20020
	ds_read_b32 v9, v8 offset:4
	v_mbcnt_lo_u32_b32 v2, -1, 0
	v_mbcnt_hi_u32_b32 v2, -1, v2
	v_readlane_b32 s6, v247, 0
	v_readlane_b32 s7, v247, 1
	s_load_dword s38, s[6:7], 0xe8
	v_readlane_b32 s39, v247, 6
	s_waitcnt lgkmcnt(0)
	v_readfirstlane_b32 s5, v9
	s_mov_b32 s37, 0
	s_cmp_ge_u32 s5, 64
	s_cbranch_scc0 .Lsf15_go
	s_mov_b32 s37, 1
	s_add_i32 s5, s39, s38
	s_cmpk_ge_u32 s5, 0x100
	s_cbranch_scc1 .Lsf15_skip
.Lsf15_go:
	s_add_i32 s5, s4, -1
	s_lshl_b32 s5, s5, 14
	v_lshl_add_u32 v7, v2, 4, s5
	ds_write_b128 v7, v[160:163] offset:0
	ds_write_b128 v7, v[164:167] offset:1024
	ds_write_b128 v7, v[168:171] offset:2048
	ds_write_b128 v7, v[172:175] offset:3072
	ds_write_b128 v7, v[176:179] offset:4096
	ds_write_b128 v7, v[180:183] offset:5120
	ds_write_b128 v7, v[184:187] offset:6144
	ds_write_b128 v7, v[188:191] offset:7168
	ds_write_b128 v7, v[192:195] offset:8192
	ds_write_b128 v7, v[196:199] offset:9216
	ds_write_b128 v7, v[200:203] offset:10240
	ds_write_b128 v7, v[204:207] offset:11264
	ds_write_b128 v7, v[208:211] offset:12288
	ds_write_b128 v7, v[212:215] offset:13312
	ds_write_b128 v7, v[216:219] offset:14336
	ds_write_b128 v7, v[220:223] offset:15360
	v_readlane_b32 s6, v247, 0
	v_readlane_b32 s7, v247, 1
	s_load_dwordx2 s[10:11], s[6:7], 0xc0
	s_load_dwordx2 s[12:13], s[6:7], 0xc8
	v_readlane_b32 s33, v247, 6
	v_mov_b32_e32 v3, 0x43e00000
	v_cmp_eq_u32_e32 vcc, 0, v2
	s_mul_i32 s33, s33, 64
	s_nop 1
	v_cndmask_b32_e64 v18, 0, 1, vcc
	s_waitcnt lgkmcnt(0)
.Lsf15_loop:
	s_cmp_eq_u32 s37, 0
	s_cbranch_scc0 .Lsf15_orph
	ds_add_rtn_u32 v9, v8, v18 offset:4
	s_waitcnt lgkmcnt(0)
	v_readfirstlane_b32 s18, v9
	s_cmp_ge_u32 s18, 64
	s_cbranch_scc0 .Lsf15_own
	s_mov_b32 s37, 1
	s_branch .Lsf15_loop
.Lsf15_own:
	s_add_i32 s18, s18, s33
	s_branch .Lsf15_unit
.Lsf15_orph:
	ds_add_rtn_u32 v9, v8, v18 offset:8
	s_waitcnt lgkmcnt(0)
	v_readfirstlane_b32 s18, v9
	s_mul_hi_u32 s35, s18, 0x4000000
	s_mul_i32 s36, s35, 64
	s_sub_i32 s36, s18, s36
	s_add_i32 s35, s35, 1
	s_mul_i32 s35, s35, s38
	s_add_i32 s35, s35, s39
	s_cmpk_ge_u32 s35, 0x100
	s_cbranch_scc1 .Lsf15_done
	s_mul_i32 s35, s35, 64
	s_add_i32 s18, s35, s36
.Lsf15_unit:
	s_and_b32 s27, s18, 1
	s_lshr_b32 s19, s18, 1
	s_add_i32 s19, s19, 0x6800
	s_cmp_lt_u32 s19, 0x7000
	s_cbranch_scc0 .Lsf15_down
	s_add_i32 s20, s19, 0xffffc800
	s_lshr_b32 s21, s20, 8
	s_mul_i32 s21, s21, 37
	s_lshr_b32 s21, s21, 8
	s_mul_i32 s28, s21, 0x700
	s_sub_i32 s20, s20, s28
	s_mul_i32 s28, s21, 0x3800000
	s_add_u32 s14, s10, s28
	s_addc_u32 s15, s11, 0
	s_mul_i32 s28, s21, 0x1c00000
	s_add_u32 s28, s28, 0x7800000
	s_add_u32 s16, s86, s28
	s_addc_u32 s17, s87, 0
	s_movk_i32 s24, 0x7000
	s_movk_i32 s25, 0x800
	s_mov_b32 s26, 0x43800000
	s_lshr_b32 s22, s20, 4
	s_mul_i32 s22, s22, 0x2493
	s_lshr_b32 s22, s22, 16
	s_mul_i32 s28, s22, 0x70
	s_sub_i32 s23, s20, s28
	s_mov_b32 s29, 1
	s_branch .Lsf15_dec
